# NA mask step 3: window mask read from an LDS {0,-inf} table (one extra ds_read per element) replacing add/and+cmp+cndmask per element; scores updated in place; on top of v15
# speedup vs baseline: 1.0173x; 1.0011x over previous
.LBB0_528:
	s_or_b64 exec, exec, s[4:5]
	v_mbcnt_lo_u32_b32 v18, -1, 0
	v_mbcnt_hi_u32_b32 v18, -1, v18
	v_cmp_gt_u32_e32 vcc, 16, v18
	v_lshlrev_b32_e32 v19, 2, v18
	v_add_u32_e32 v19, 0x16000, v19
	v_cndmask_b32_e64 v20, v242, 0, vcc
	ds_write_b32 v19, v242
	ds_write_b32 v19, v20 offset:256
	s_and_b32 s4, s0, 0x3fffffc0
	s_ashr_i32 s65, s0, 7
	s_lshl_b32 s0, s4, 2
	s_add_i32 s6, s0, 0
	s_max_i32 s0, s63, 1
	s_add_i32 s0, s0, -1
	s_min_u32 s12, s0, 56
	s_add_i32 s12, s12, 7
	s_sub_i32 s7, s12, s1
	s_add_i32 s0, s7, 5
	s_and_b32 s13, s0, 1
	s_max_i32 s46, s57, 4
	s_add_i32 s0, s13, s0
	s_cmp_lg_u32 0, -1
	s_cselect_b32 s4, 0, 0
	v_lshlrev_b32_e32 v0, 10, v216
	v_lshlrev_b32_e32 v18, 4, v213
	s_add_i32 s4, s4, s23
	v_add3_u32 v227, 0, v0, v18
	v_lshl_add_u64 v[18:19], v[36:37], 0, s[20:21]
	s_add_i32 s5, s4, 0x4000
	s_mov_b32 s23, m0
	s_mov_b32 m0, s5
	s_nop 0
	global_load_lds_dwordx4 v[18:19], off
	s_mov_b32 m0, s23
	s_waitcnt vmcnt(3) lgkmcnt(0)
	s_barrier
	ds_read_b128 v[40:43], v227
	ds_read_b128 v[44:47], v227 offset:512
	s_waitcnt vmcnt(1) lgkmcnt(1)
	v_mfma_f32_32x32x16_bf16 v[18:33], v[40:43], v[156:159], v[2:17]
	v_and_or_b32 v39, s59, 32, v213
	v_sub_u32_e32 v224, 15, v39
	s_mov_b64 s[26:27], 0x288000
	s_add_i32 s4, s4, 0x8000
	v_lshlrev_b32_e32 v0, 1, v38
	v_and_b32_e32 v219, 32, v0
	v_lshlrev_b32_e32 v0, 2, v216
	s_waitcnt lgkmcnt(0)
	v_mfma_f32_32x32x16_bf16 v[2:17], v[44:47], v[156:159], v[2:17]
	ds_read_b128 v[40:43], v227 offset:2048
	ds_read_b128 v[44:47], v227 offset:2560
	v_lshrrev_b32_e32 v38, 2, v38
	v_and_or_b32 v38, v38, 3, v0
	v_lshlrev_b32_e32 v218, 6, v38
	v_add_u32_e32 v38, 0, v219
	v_add3_u32 v226, v38, v217, v218
	v_lshl_add_u32 v225, v216, 4, s77
	s_waitcnt lgkmcnt(1)
	v_mfma_f32_32x32x16_bf16 v[18:33], v[40:43], v[152:155], v[18:33]
	s_mov_b32 s23, 1
	s_mov_b32 s47, 0
	s_movk_i32 s81, 0x4000
	s_cmp_gt_i32 s0, 6
	v_lshl_add_u32 v228, v224, 2, v225
	v_lshl_add_u64 v[196:197], v[34:35], 0, s[2:3]
	v_lshl_add_u32 v221, v213, 2, s6
	s_waitcnt lgkmcnt(0)
	v_mfma_f32_32x32x16_bf16 v[2:17], v[44:47], v[152:155], v[2:17]
	ds_read_b128 v[40:43], v227 offset:4096
	ds_read_b128 v[44:47], v227 offset:4608
	v_lshl_add_u32 v220, v0, 2, s6
	s_waitcnt lgkmcnt(1)
	v_mfma_f32_32x32x16_bf16 v[18:33], v[40:43], v[148:151], v[18:33]
	ds_read_b128 v[40:43], v227 offset:6656
	ds_read_b128 v[48:51], v227 offset:6144
	s_waitcnt lgkmcnt(2)
	v_mfma_f32_32x32x16_bf16 v[2:17], v[44:47], v[148:151], v[2:17]
	v_sub_u32_e64 v44, v39, 8 clamp
	v_min_u32_e32 v38, 48, v44
	v_sub_u32_e32 v223, v0, v38
	s_waitcnt vmcnt(0) lgkmcnt(0)
	v_mfma_f32_32x32x16_bf16 v[18:33], v[48:51], v[144:147], v[18:33]
	v_mfma_f32_32x32x16_bf16 v[2:17], v[40:43], v[144:147], v[2:17]
	s_nop 15
	s_nop 7
	s_nop 0
	v_max3_f32 v39, v18, v19, v2
	v_max3_f32 v40, v20, v21, v3
	s_nop 0
	v_max3_f32 v39, v39, v4, v5
	v_max3_f32 v40, v40, v24, v25
	s_nop 0
	v_max3_f32 v39, v39, v22, v23
	v_max3_f32 v40, v40, v8, v9
	s_nop 0
	v_max3_f32 v39, v39, v6, v7
	v_max3_f32 v40, v40, v28, v29
	s_nop 0
	v_max3_f32 v39, v39, v26, v27
	v_max3_f32 v40, v40, v12, v13
	s_nop 0
	v_max3_f32 v39, v39, v10, v11
	v_max3_f32 v40, v40, v32, v33
	s_nop 0
	v_max3_f32 v39, v39, v30, v31
	v_max3_f32 v40, v40, v16, v17
	s_nop 0
	v_max3_f32 v39, v39, v14, v15
	s_nop 0
	v_max_f32_e32 v39, v39, v40
	s_nop 0
	v_mov_b32_e32 v40, v39
	s_nop 1
	v_permlane32_swap_b32_e32 v39, v40
	v_max_f32_e32 v39, v39, v40
	s_nop 0
	v_add_f32_e32 v222, v1, v39
	v_sub_f32_e32 v2, v2, v39
	v_sub_f32_e32 v3, v3, v39
	v_sub_f32_e32 v18, v18, v39
	v_sub_f32_e32 v19, v19, v39
	v_sub_f32_e32 v20, v20, v39
	s_nop 0
	v_xor_b32_e32 v48, 0x80000000, v222
	v_mov_b32_e32 v49, v48
	v_mov_b32_e32 v50, v48
	v_mov_b32_e32 v51, v48
	v_mov_b32_e32 v52, v48
	v_mov_b32_e32 v53, v48
	v_mov_b32_e32 v54, v48
	v_mov_b32_e32 v55, v48
	v_mov_b32_e32 v56, v48
	v_mov_b32_e32 v57, v48
	v_mov_b32_e32 v58, v48
	v_mov_b32_e32 v59, v48
	v_mov_b32_e32 v60, v48
	v_mov_b32_e32 v61, v48
	v_mov_b32_e32 v62, v48
	v_mov_b32_e32 v63, v48
	s_waitcnt vmcnt(0) lgkmcnt(0)
	s_barrier
	v_exp_f32_e32 v64, v2
	v_exp_f32_e32 v65, v3
	v_lshl_add_u64 v[2:3], v[36:37], 0, s[26:27]
	s_mov_b32 s5, m0
	s_mov_b32 m0, s8
	s_nop 0
	global_load_lds_dwordx4 v[2:3], off
	s_mov_b32 m0, s5
	v_lshl_add_u64 v[2:3], v[204:205], 0, s[70:71]
	s_mov_b32 s5, m0
	s_mov_b32 m0, s4
	s_nop 0
	global_load_lds_dwordx4 v[2:3], off
	s_mov_b32 m0, s5
	ds_read_b128 v[188:191], v227 offset:8192
	ds_read_b128 v[184:187], v227 offset:8704
	ds_read_b128 v[180:183], v227 offset:10240
	ds_read_b128 v[176:179], v227 offset:10752
	ds_read_b128 v[172:175], v227 offset:12288
	ds_read_b128 v[168:171], v227 offset:12800
	ds_read_b128 v[164:167], v227 offset:14336
	ds_read_b128 v[160:163], v227 offset:14848
	v_sub_f32_e32 v4, v4, v39
	v_sub_f32_e32 v21, v21, v39
	v_sub_f32_e32 v5, v5, v39
	v_sub_f32_e32 v22, v22, v39
	v_sub_f32_e32 v6, v6, v39
	v_sub_f32_e32 v23, v23, v39
	v_sub_f32_e32 v7, v7, v39
	v_sub_f32_e32 v24, v24, v39
	v_sub_f32_e32 v8, v8, v39
	v_sub_f32_e32 v25, v25, v39
	v_sub_f32_e32 v9, v9, v39
	v_sub_f32_e32 v26, v26, v39
	v_sub_f32_e32 v10, v10, v39
	v_sub_f32_e32 v27, v27, v39
	v_sub_f32_e32 v11, v11, v39
	v_sub_f32_e32 v28, v28, v39
	v_sub_f32_e32 v12, v12, v39
	v_sub_f32_e32 v29, v29, v39
	v_sub_f32_e32 v13, v13, v39
	v_sub_f32_e32 v30, v30, v39
	v_sub_f32_e32 v14, v14, v39
	v_sub_f32_e32 v31, v31, v39
	v_sub_f32_e32 v15, v15, v39
	v_sub_f32_e32 v32, v32, v39
	v_sub_f32_e32 v16, v16, v39
	v_sub_f32_e32 v33, v33, v39
	v_sub_f32_e32 v17, v17, v39
	v_exp_f32_e32 v80, v18
	v_exp_f32_e32 v81, v19
	v_exp_f32_e32 v82, v20
	v_exp_f32_e32 v83, v21
	v_exp_f32_e32 v84, v22
	v_exp_f32_e32 v85, v23
	v_exp_f32_e32 v86, v24
	v_exp_f32_e32 v87, v25
	v_exp_f32_e32 v88, v26
	v_exp_f32_e32 v89, v27
	v_exp_f32_e32 v90, v28
	v_exp_f32_e32 v91, v29
	v_exp_f32_e32 v92, v30
	v_exp_f32_e32 v93, v31
	v_exp_f32_e32 v94, v32
	v_exp_f32_e32 v95, v33
	v_exp_f32_e32 v66, v4
	v_exp_f32_e32 v67, v5
	v_exp_f32_e32 v68, v6
	v_exp_f32_e32 v69, v7
	v_exp_f32_e32 v70, v8
	v_exp_f32_e32 v71, v9
	v_exp_f32_e32 v72, v10
	v_exp_f32_e32 v73, v11
	v_exp_f32_e32 v74, v12
	v_exp_f32_e32 v75, v13
	v_exp_f32_e32 v76, v14
	v_exp_f32_e32 v77, v15
	v_exp_f32_e32 v78, v16
	v_exp_f32_e32 v79, v17
	s_waitcnt vmcnt(2) lgkmcnt(0)
	s_barrier
	v_cmp_gt_u32_e64 s[4:5], 32, v211
	s_cbranch_scc0 .LBB0_618
	s_mul_i32 s6, s46, 0xd8000
	s_add_i32 s68, s6, 0xffca0000
	s_add_i32 s6, s46, s56
	s_sub_i32 s49, s6, s65
	s_add_i32 s6, s65, s57
	s_max_i32 s6, s6, 4
	s_add_i32 s6, s6, -4
	v_mov_b32_e32 v14, v1
	v_mov_b32_e32 v15, v1
	s_min_u32 s6, s6, 56
	v_mov_b32_e32 v0, v1
	v_mov_b32_e32 v2, v1
	v_mov_b32_e32 v3, v1
	v_mov_b32_e32 v4, v1
	v_mov_b32_e32 v5, v1
	v_mov_b32_e32 v6, v1
	v_mov_b32_e32 v7, v1
	v_mov_b32_e32 v8, v1
	v_mov_b32_e32 v9, v1
	v_mov_b32_e32 v10, v1
	v_mov_b32_e32 v11, v1
	v_mov_b32_e32 v12, v1
	v_mov_b32_e32 v13, v1
	v_mov_b64_e32 v[46:47], v[14:15]
	v_mov_b64_e32 v[30:31], v[14:15]
	s_add_i32 s48, s13, s7
	s_sub_i32 s50, s46, s6
	v_lshl_add_u64 v[198:199], v[196:197], 0, s[68:69]
	s_mov_b32 s44, 0
	s_movk_i32 s47, 0x4000
	s_movk_i32 s64, 0x2000
	v_mov_b32_e32 v229, 0
	s_mov_b32 s23, -2
	s_mov_b64 s[6:7], s[72:73]
	v_mov_b64_e32 v[44:45], v[12:13]
	v_mov_b64_e32 v[42:43], v[10:11]
	v_mov_b64_e32 v[40:41], v[8:9]
	v_mov_b64_e32 v[38:39], v[6:7]
	v_mov_b64_e32 v[36:37], v[4:5]
	v_mov_b64_e32 v[34:35], v[2:3]
	v_mov_b64_e32 v[32:33], v[0:1]
	v_mov_b64_e32 v[28:29], v[12:13]
	v_mov_b64_e32 v[26:27], v[10:11]
	v_mov_b64_e32 v[24:25], v[8:9]
	v_mov_b64_e32 v[22:23], v[6:7]
	v_mov_b64_e32 v[20:21], v[4:5]
	v_mov_b64_e32 v[18:19], v[2:3]
	v_mov_b64_e32 v[16:17], v[0:1]

.LBB0_534:
	v_mad_u64_u32 v[14:15], s[44:45], s42, v241, v[204:205]
	s_mul_i32 s27, s43, 0x3600
	v_add_u32_e32 v15, s27, v15
	s_add_i32 s27, s47, s9
	s_mov_b32 s42, m0
	s_mov_b32 m0, s27
	s_nop 0
	global_load_lds_dwordx4 v[14:15], off
	s_mov_b32 m0, s42
	s_cmp_lt_u32 s26, 4
	s_cbranch_scc1 .LBB0_568
	s_add_i32 s27, s50, s23
	s_add_i32 s27, s27, -5
	s_cmp_gt_u32 s27, 7
	s_cselect_b64 vcc, -1, 0
	s_cbranch_scc1 .Lna_allmask_0
	s_add_i32 s27, s49, s23
	s_add_i32 s27, s27, -5
	s_max_i32 s27, s27, -7
	s_add_i32 s27, s27, 7
	s_min_u32 s27, s27, 14
	s_mulk_i32 s27, 0x7c
	v_add_u32_e32 v161, s27, v228
	v_mov_b32_e32 v15, v223
	v_lshlrev_b32_e32 v76, 2, v223
	v_add_u32_e32 v76, 0x16100, v76
	ds_read_b32 v64, v161
	ds_read_b32 v70, v76
	ds_read_b32 v65, v161 offset:4
	ds_read_b32 v71, v76 offset:4
	ds_read_b32 v66, v161 offset:8
	ds_read_b32 v72, v76 offset:8
	ds_read_b32 v67, v161 offset:12
	ds_read_b32 v73, v76 offset:12
	ds_read_b32 v68, v161 offset:32
	ds_read_b32 v74, v76 offset:32
	ds_read_b32 v69, v161 offset:36
	ds_read_b32 v75, v76 offset:36
	s_waitcnt lgkmcnt(10)
	v_add_f32_e32 v112, v112, v64
	v_add_f32_e32 v112, v112, v70
	ds_read_b32 v64, v161 offset:40
	ds_read_b32 v70, v76 offset:40
	s_waitcnt lgkmcnt(10)
	v_add_f32_e32 v113, v113, v65
	v_add_f32_e32 v113, v113, v71
	ds_read_b32 v65, v161 offset:44
	ds_read_b32 v71, v76 offset:44
	s_waitcnt lgkmcnt(10)
	v_add_f32_e32 v114, v114, v66
	v_add_f32_e32 v114, v114, v72
	ds_read_b32 v66, v161 offset:64
	ds_read_b32 v72, v76 offset:64
	s_waitcnt lgkmcnt(10)
	v_add_f32_e32 v115, v115, v67
	v_add_f32_e32 v115, v115, v73
	ds_read_b32 v67, v161 offset:68
	ds_read_b32 v73, v76 offset:68
	s_waitcnt lgkmcnt(10)
	v_add_f32_e32 v116, v116, v68
	v_add_f32_e32 v116, v116, v74
	ds_read_b32 v68, v161 offset:72
	ds_read_b32 v74, v76 offset:72
	s_waitcnt lgkmcnt(10)
	v_add_f32_e32 v117, v117, v69
	v_add_f32_e32 v117, v117, v75
	ds_read_b32 v69, v161 offset:76
	ds_read_b32 v75, v76 offset:76
	s_waitcnt lgkmcnt(10)
	v_add_f32_e32 v118, v118, v64
	v_add_f32_e32 v118, v118, v70
	ds_read_b32 v64, v161 offset:96
	ds_read_b32 v70, v76 offset:96
	s_waitcnt lgkmcnt(10)
	v_add_f32_e32 v119, v119, v65
	v_add_f32_e32 v119, v119, v71
	ds_read_b32 v65, v161 offset:100
	ds_read_b32 v71, v76 offset:100
	s_waitcnt lgkmcnt(10)
	v_add_f32_e32 v120, v120, v66
	v_add_f32_e32 v120, v120, v72
	ds_read_b32 v66, v161 offset:104
	ds_read_b32 v72, v76 offset:104
	s_waitcnt lgkmcnt(10)
	v_add_f32_e32 v121, v121, v67
	v_add_f32_e32 v121, v121, v73
	ds_read_b32 v67, v161 offset:108
	ds_read_b32 v73, v76 offset:108
	s_waitcnt lgkmcnt(10)
	v_add_f32_e32 v122, v122, v68
	v_add_f32_e32 v122, v122, v74
	ds_read_b32 v68, v161 offset:128
	ds_read_b32 v74, v76 offset:128
	s_waitcnt lgkmcnt(10)
	v_add_f32_e32 v123, v123, v69
	v_add_f32_e32 v123, v123, v75
	ds_read_b32 v69, v161 offset:132
	ds_read_b32 v75, v76 offset:132
	s_waitcnt lgkmcnt(10)
	v_add_f32_e32 v124, v124, v64
	v_add_f32_e32 v124, v124, v70
	ds_read_b32 v64, v161 offset:136
	ds_read_b32 v70, v76 offset:136
	s_waitcnt lgkmcnt(10)
	v_add_f32_e32 v125, v125, v65
	v_add_f32_e32 v125, v125, v71
	ds_read_b32 v65, v161 offset:140
	ds_read_b32 v71, v76 offset:140
	s_waitcnt lgkmcnt(10)
	v_add_f32_e32 v126, v126, v66
	v_add_f32_e32 v126, v126, v72
	ds_read_b32 v66, v161 offset:160
	ds_read_b32 v72, v76 offset:160
	s_waitcnt lgkmcnt(10)
	v_add_f32_e32 v127, v127, v67
	v_add_f32_e32 v127, v127, v73
	ds_read_b32 v67, v161 offset:164
	ds_read_b32 v73, v76 offset:164
	s_waitcnt lgkmcnt(10)
	v_add_f32_e32 v96, v96, v68
	v_add_f32_e32 v96, v96, v74
	ds_read_b32 v68, v161 offset:168
	ds_read_b32 v74, v76 offset:168
	s_waitcnt lgkmcnt(10)
	v_add_f32_e32 v97, v97, v69
	v_add_f32_e32 v97, v97, v75
	ds_read_b32 v69, v161 offset:172
	ds_read_b32 v75, v76 offset:172
	s_waitcnt lgkmcnt(10)
	v_add_f32_e32 v98, v98, v64
	v_add_f32_e32 v98, v98, v70
	ds_read_b32 v64, v161 offset:192
	ds_read_b32 v70, v76 offset:192
	s_waitcnt lgkmcnt(10)
	v_add_f32_e32 v99, v99, v65
	v_add_f32_e32 v99, v99, v71
	ds_read_b32 v65, v161 offset:196
	ds_read_b32 v71, v76 offset:196
	s_waitcnt lgkmcnt(10)
	v_add_f32_e32 v100, v100, v66
	v_add_f32_e32 v100, v100, v72
	ds_read_b32 v66, v161 offset:200
	ds_read_b32 v72, v76 offset:200
	s_waitcnt lgkmcnt(10)
	v_add_f32_e32 v101, v101, v67
	v_add_f32_e32 v101, v101, v73
	ds_read_b32 v67, v161 offset:204
	ds_read_b32 v73, v76 offset:204
	s_waitcnt lgkmcnt(10)
	v_add_f32_e32 v102, v102, v68
	v_add_f32_e32 v102, v102, v74
	ds_read_b32 v68, v161 offset:224
	ds_read_b32 v74, v76 offset:224
	s_waitcnt lgkmcnt(10)
	v_add_f32_e32 v103, v103, v69
	v_add_f32_e32 v103, v103, v75
	ds_read_b32 v69, v161 offset:228
	ds_read_b32 v75, v76 offset:228
	s_waitcnt lgkmcnt(10)
	v_add_f32_e32 v104, v104, v64
	v_add_f32_e32 v104, v104, v70
	ds_read_b32 v64, v161 offset:232
	ds_read_b32 v70, v76 offset:232
	s_waitcnt lgkmcnt(10)
	v_add_f32_e32 v105, v105, v65
	v_add_f32_e32 v105, v105, v71
	ds_read_b32 v65, v161 offset:236
	ds_read_b32 v71, v76 offset:236
	s_waitcnt lgkmcnt(10)
	v_add_f32_e32 v106, v106, v66
	v_add_f32_e32 v106, v106, v72
	s_waitcnt lgkmcnt(8)
	v_add_f32_e32 v107, v107, v67
	v_add_f32_e32 v107, v107, v73
	s_waitcnt lgkmcnt(6)
	v_add_f32_e32 v108, v108, v68
	v_add_f32_e32 v108, v108, v74
	s_waitcnt lgkmcnt(4)
	v_add_f32_e32 v109, v109, v69
	v_add_f32_e32 v109, v109, v75
	s_waitcnt lgkmcnt(2)
	v_add_f32_e32 v110, v110, v64
	v_add_f32_e32 v110, v110, v70
	s_waitcnt lgkmcnt(0)
	v_add_f32_e32 v111, v111, v65
	v_add_f32_e32 v111, v111, v71
	s_branch .LBB0_568

.LBB0_573:
	s_add_i32 s27, s47, 0x2000
	s_cmpk_lg_i32 s47, 0x4000
	s_cselect_b32 s64, s27, 0
	v_mad_u64_u32 v[96:97], s[44:45], s42, v241, v[204:205]
	s_mul_i32 s27, s43, 0x3600
	v_add_u32_e32 v97, s27, v97
	s_add_i32 s27, s64, s9
	s_cmp_lt_u32 s26, 3
	s_mov_b32 s26, m0
	s_mov_b32 m0, s27
	s_nop 0
	global_load_lds_dwordx4 v[96:97], off
	s_mov_b32 m0, s26
	s_cbranch_scc1 .LBB0_607
	s_add_i32 s26, s50, s23
	s_add_i32 s26, s26, -4
	s_cmp_gt_u32 s26, 7
	s_cselect_b64 vcc, -1, 0
	s_cbranch_scc1 .Lna_allmask_1
	s_add_i32 s26, s49, s23
	s_add_i32 s26, s26, -4
	s_max_i32 s26, s26, -7
	s_add_i32 s26, s26, 7
	s_min_u32 s26, s26, 14
	s_mulk_i32 s26, 0x7c
	v_add_u32_e32 v166, s26, v228
	v_mov_b32_e32 v164, v223
	v_lshlrev_b32_e32 v108, 2, v223
	v_add_u32_e32 v108, 0x16100, v108
	ds_read_b32 v96, v166
	ds_read_b32 v102, v108
	ds_read_b32 v97, v166 offset:4
	ds_read_b32 v103, v108 offset:4
	ds_read_b32 v98, v166 offset:8
	ds_read_b32 v104, v108 offset:8
	ds_read_b32 v99, v166 offset:12
	ds_read_b32 v105, v108 offset:12
	ds_read_b32 v100, v166 offset:32
	ds_read_b32 v106, v108 offset:32
	ds_read_b32 v101, v166 offset:36
	ds_read_b32 v107, v108 offset:36
	s_waitcnt lgkmcnt(10)
	v_add_f32_e32 v80, v80, v96
	v_add_f32_e32 v80, v80, v102
	ds_read_b32 v96, v166 offset:40
	ds_read_b32 v102, v108 offset:40
	s_waitcnt lgkmcnt(10)
	v_add_f32_e32 v81, v81, v97
	v_add_f32_e32 v81, v81, v103
	ds_read_b32 v97, v166 offset:44
	ds_read_b32 v103, v108 offset:44
	s_waitcnt lgkmcnt(10)
	v_add_f32_e32 v82, v82, v98
	v_add_f32_e32 v82, v82, v104
	ds_read_b32 v98, v166 offset:64
	ds_read_b32 v104, v108 offset:64
	s_waitcnt lgkmcnt(10)
	v_add_f32_e32 v83, v83, v99
	v_add_f32_e32 v83, v83, v105
	ds_read_b32 v99, v166 offset:68
	ds_read_b32 v105, v108 offset:68
	s_waitcnt lgkmcnt(10)
	v_add_f32_e32 v84, v84, v100
	v_add_f32_e32 v84, v84, v106
	ds_read_b32 v100, v166 offset:72
	ds_read_b32 v106, v108 offset:72
	s_waitcnt lgkmcnt(10)
	v_add_f32_e32 v85, v85, v101
	v_add_f32_e32 v85, v85, v107
	ds_read_b32 v101, v166 offset:76
	ds_read_b32 v107, v108 offset:76
	s_waitcnt lgkmcnt(10)
	v_add_f32_e32 v86, v86, v96
	v_add_f32_e32 v86, v86, v102
	ds_read_b32 v96, v166 offset:96
	ds_read_b32 v102, v108 offset:96
	s_waitcnt lgkmcnt(10)
	v_add_f32_e32 v87, v87, v97
	v_add_f32_e32 v87, v87, v103
	ds_read_b32 v97, v166 offset:100
	ds_read_b32 v103, v108 offset:100
	s_waitcnt lgkmcnt(10)
	v_add_f32_e32 v88, v88, v98
	v_add_f32_e32 v88, v88, v104
	ds_read_b32 v98, v166 offset:104
	ds_read_b32 v104, v108 offset:104
	s_waitcnt lgkmcnt(10)
	v_add_f32_e32 v89, v89, v99
	v_add_f32_e32 v89, v89, v105
	ds_read_b32 v99, v166 offset:108
	ds_read_b32 v105, v108 offset:108
	s_waitcnt lgkmcnt(10)
	v_add_f32_e32 v90, v90, v100
	v_add_f32_e32 v90, v90, v106
	ds_read_b32 v100, v166 offset:128
	ds_read_b32 v106, v108 offset:128
	s_waitcnt lgkmcnt(10)
	v_add_f32_e32 v91, v91, v101
	v_add_f32_e32 v91, v91, v107
	ds_read_b32 v101, v166 offset:132
	ds_read_b32 v107, v108 offset:132
	s_waitcnt lgkmcnt(10)
	v_add_f32_e32 v92, v92, v96
	v_add_f32_e32 v92, v92, v102
	ds_read_b32 v96, v166 offset:136
	ds_read_b32 v102, v108 offset:136
	s_waitcnt lgkmcnt(10)
	v_add_f32_e32 v93, v93, v97
	v_add_f32_e32 v93, v93, v103
	ds_read_b32 v97, v166 offset:140
	ds_read_b32 v103, v108 offset:140
	s_waitcnt lgkmcnt(10)
	v_add_f32_e32 v94, v94, v98
	v_add_f32_e32 v94, v94, v104
	ds_read_b32 v98, v166 offset:160
	ds_read_b32 v104, v108 offset:160
	s_waitcnt lgkmcnt(10)
	v_add_f32_e32 v95, v95, v99
	v_add_f32_e32 v95, v95, v105
	ds_read_b32 v99, v166 offset:164
	ds_read_b32 v105, v108 offset:164
	s_waitcnt lgkmcnt(10)
	v_add_f32_e32 v64, v64, v100
	v_add_f32_e32 v64, v64, v106
	ds_read_b32 v100, v166 offset:168
	ds_read_b32 v106, v108 offset:168
	s_waitcnt lgkmcnt(10)
	v_add_f32_e32 v65, v65, v101
	v_add_f32_e32 v65, v65, v107
	ds_read_b32 v101, v166 offset:172
	ds_read_b32 v107, v108 offset:172
	s_waitcnt lgkmcnt(10)
	v_add_f32_e32 v66, v66, v96
	v_add_f32_e32 v66, v66, v102
	ds_read_b32 v96, v166 offset:192
	ds_read_b32 v102, v108 offset:192
	s_waitcnt lgkmcnt(10)
	v_add_f32_e32 v67, v67, v97
	v_add_f32_e32 v67, v67, v103
	ds_read_b32 v97, v166 offset:196
	ds_read_b32 v103, v108 offset:196
	s_waitcnt lgkmcnt(10)
	v_add_f32_e32 v68, v68, v98
	v_add_f32_e32 v68, v68, v104
	ds_read_b32 v98, v166 offset:200
	ds_read_b32 v104, v108 offset:200
	s_waitcnt lgkmcnt(10)
	v_add_f32_e32 v69, v69, v99
	v_add_f32_e32 v69, v69, v105
	ds_read_b32 v99, v166 offset:204
	ds_read_b32 v105, v108 offset:204
	s_waitcnt lgkmcnt(10)
	v_add_f32_e32 v70, v70, v100
	v_add_f32_e32 v70, v70, v106
	ds_read_b32 v100, v166 offset:224
	ds_read_b32 v106, v108 offset:224
	s_waitcnt lgkmcnt(10)
	v_add_f32_e32 v71, v71, v101
	v_add_f32_e32 v71, v71, v107
	ds_read_b32 v101, v166 offset:228
	ds_read_b32 v107, v108 offset:228
	s_waitcnt lgkmcnt(10)
	v_add_f32_e32 v72, v72, v96
	v_add_f32_e32 v72, v72, v102
	ds_read_b32 v96, v166 offset:232
	ds_read_b32 v102, v108 offset:232
	s_waitcnt lgkmcnt(10)
	v_add_f32_e32 v73, v73, v97
	v_add_f32_e32 v73, v73, v103
	ds_read_b32 v97, v166 offset:236
	ds_read_b32 v103, v108 offset:236
	s_waitcnt lgkmcnt(10)
	v_add_f32_e32 v74, v74, v98
	v_add_f32_e32 v74, v74, v104
	s_waitcnt lgkmcnt(8)
	v_add_f32_e32 v75, v75, v99
	v_add_f32_e32 v75, v75, v105
	s_waitcnt lgkmcnt(6)
	v_add_f32_e32 v76, v76, v100
	v_add_f32_e32 v76, v76, v106
	s_waitcnt lgkmcnt(4)
	v_add_f32_e32 v77, v77, v101
	v_add_f32_e32 v77, v77, v107
	s_waitcnt lgkmcnt(2)
	v_add_f32_e32 v78, v78, v96
	v_add_f32_e32 v78, v78, v102
	s_waitcnt lgkmcnt(0)
	v_add_f32_e32 v79, v79, v97
	v_add_f32_e32 v79, v79, v103
	s_branch .LBB0_607

.LBB0_625:
	v_mad_u64_u32 v[64:65], s[46:47], s6, v241, v[204:205]
	s_mul_i32 s6, s7, 0x3600
	v_add_u32_e32 v65, s6, v65
	s_add_i32 s6, s81, s9
	s_mov_b32 s7, m0
	s_mov_b32 m0, s6
	s_nop 0
	global_load_lds_dwordx4 v[64:65], off
	s_mov_b32 m0, s7
	s_cmp_lt_u32 s50, 4
	s_cbranch_scc1 .LBB0_659
	s_add_i32 s6, s23, s90
	s_add_i32 s6, s6, -8
	s_cmp_gt_u32 s6, 7
	s_cselect_b64 vcc, -1, 0
	s_cbranch_scc1 .Lna_allmask_2
	s_add_i32 s6, s23, s74
	s_max_i32 s6, s6, -7
	s_add_i32 s6, s6, 7
	s_min_u32 s6, s6, 14
	s_mulk_i32 s6, 0x7c
	v_add_u32_e32 v163, s6, v228
	v_mov_b32_e32 v161, v223
	v_lshlrev_b32_e32 v76, 2, v223
	v_add_u32_e32 v76, 0x16100, v76
	ds_read_b32 v64, v163
	ds_read_b32 v70, v76
	ds_read_b32 v65, v163 offset:4
	ds_read_b32 v71, v76 offset:4
	ds_read_b32 v66, v163 offset:8
	ds_read_b32 v72, v76 offset:8
	ds_read_b32 v67, v163 offset:12
	ds_read_b32 v73, v76 offset:12
	ds_read_b32 v68, v163 offset:32
	ds_read_b32 v74, v76 offset:32
	ds_read_b32 v69, v163 offset:36
	ds_read_b32 v75, v76 offset:36
	s_waitcnt lgkmcnt(10)
	v_add_f32_e32 v112, v112, v64
	v_add_f32_e32 v112, v112, v70
	ds_read_b32 v64, v163 offset:40
	ds_read_b32 v70, v76 offset:40
	s_waitcnt lgkmcnt(10)
	v_add_f32_e32 v113, v113, v65
	v_add_f32_e32 v113, v113, v71
	ds_read_b32 v65, v163 offset:44
	ds_read_b32 v71, v76 offset:44
	s_waitcnt lgkmcnt(10)
	v_add_f32_e32 v114, v114, v66
	v_add_f32_e32 v114, v114, v72
	ds_read_b32 v66, v163 offset:64
	ds_read_b32 v72, v76 offset:64
	s_waitcnt lgkmcnt(10)
	v_add_f32_e32 v115, v115, v67
	v_add_f32_e32 v115, v115, v73
	ds_read_b32 v67, v163 offset:68
	ds_read_b32 v73, v76 offset:68
	s_waitcnt lgkmcnt(10)
	v_add_f32_e32 v116, v116, v68
	v_add_f32_e32 v116, v116, v74
	ds_read_b32 v68, v163 offset:72
	ds_read_b32 v74, v76 offset:72
	s_waitcnt lgkmcnt(10)
	v_add_f32_e32 v117, v117, v69
	v_add_f32_e32 v117, v117, v75
	ds_read_b32 v69, v163 offset:76
	ds_read_b32 v75, v76 offset:76
	s_waitcnt lgkmcnt(10)
	v_add_f32_e32 v118, v118, v64
	v_add_f32_e32 v118, v118, v70
	ds_read_b32 v64, v163 offset:96
	ds_read_b32 v70, v76 offset:96
	s_waitcnt lgkmcnt(10)
	v_add_f32_e32 v119, v119, v65
	v_add_f32_e32 v119, v119, v71
	ds_read_b32 v65, v163 offset:100
	ds_read_b32 v71, v76 offset:100
	s_waitcnt lgkmcnt(10)
	v_add_f32_e32 v120, v120, v66
	v_add_f32_e32 v120, v120, v72
	ds_read_b32 v66, v163 offset:104
	ds_read_b32 v72, v76 offset:104
	s_waitcnt lgkmcnt(10)
	v_add_f32_e32 v121, v121, v67
	v_add_f32_e32 v121, v121, v73
	ds_read_b32 v67, v163 offset:108
	ds_read_b32 v73, v76 offset:108
	s_waitcnt lgkmcnt(10)
	v_add_f32_e32 v122, v122, v68
	v_add_f32_e32 v122, v122, v74
	ds_read_b32 v68, v163 offset:128
	ds_read_b32 v74, v76 offset:128
	s_waitcnt lgkmcnt(10)
	v_add_f32_e32 v123, v123, v69
	v_add_f32_e32 v123, v123, v75
	ds_read_b32 v69, v163 offset:132
	ds_read_b32 v75, v76 offset:132
	s_waitcnt lgkmcnt(10)
	v_add_f32_e32 v124, v124, v64
	v_add_f32_e32 v124, v124, v70
	ds_read_b32 v64, v163 offset:136
	ds_read_b32 v70, v76 offset:136
	s_waitcnt lgkmcnt(10)
	v_add_f32_e32 v125, v125, v65
	v_add_f32_e32 v125, v125, v71
	ds_read_b32 v65, v163 offset:140
	ds_read_b32 v71, v76 offset:140
	s_waitcnt lgkmcnt(10)
	v_add_f32_e32 v126, v126, v66
	v_add_f32_e32 v126, v126, v72
	ds_read_b32 v66, v163 offset:160
	ds_read_b32 v72, v76 offset:160
	s_waitcnt lgkmcnt(10)
	v_add_f32_e32 v127, v127, v67
	v_add_f32_e32 v127, v127, v73
	ds_read_b32 v67, v163 offset:164
	ds_read_b32 v73, v76 offset:164
	s_waitcnt lgkmcnt(10)
	v_add_f32_e32 v96, v96, v68
	v_add_f32_e32 v96, v96, v74
	ds_read_b32 v68, v163 offset:168
	ds_read_b32 v74, v76 offset:168
	s_waitcnt lgkmcnt(10)
	v_add_f32_e32 v97, v97, v69
	v_add_f32_e32 v97, v97, v75
	ds_read_b32 v69, v163 offset:172
	ds_read_b32 v75, v76 offset:172
	s_waitcnt lgkmcnt(10)
	v_add_f32_e32 v98, v98, v64
	v_add_f32_e32 v98, v98, v70
	ds_read_b32 v64, v163 offset:192
	ds_read_b32 v70, v76 offset:192
	s_waitcnt lgkmcnt(10)
	v_add_f32_e32 v99, v99, v65
	v_add_f32_e32 v99, v99, v71
	ds_read_b32 v65, v163 offset:196
	ds_read_b32 v71, v76 offset:196
	s_waitcnt lgkmcnt(10)
	v_add_f32_e32 v100, v100, v66
	v_add_f32_e32 v100, v100, v72
	ds_read_b32 v66, v163 offset:200
	ds_read_b32 v72, v76 offset:200
	s_waitcnt lgkmcnt(10)
	v_add_f32_e32 v101, v101, v67
	v_add_f32_e32 v101, v101, v73
	ds_read_b32 v67, v163 offset:204
	ds_read_b32 v73, v76 offset:204
	s_waitcnt lgkmcnt(10)
	v_add_f32_e32 v102, v102, v68
	v_add_f32_e32 v102, v102, v74
	ds_read_b32 v68, v163 offset:224
	ds_read_b32 v74, v76 offset:224
	s_waitcnt lgkmcnt(10)
	v_add_f32_e32 v103, v103, v69
	v_add_f32_e32 v103, v103, v75
	ds_read_b32 v69, v163 offset:228
	ds_read_b32 v75, v76 offset:228
	s_waitcnt lgkmcnt(10)
	v_add_f32_e32 v104, v104, v64
	v_add_f32_e32 v104, v104, v70
	ds_read_b32 v64, v163 offset:232
	ds_read_b32 v70, v76 offset:232
	s_waitcnt lgkmcnt(10)
	v_add_f32_e32 v105, v105, v65
	v_add_f32_e32 v105, v105, v71
	ds_read_b32 v65, v163 offset:236
	ds_read_b32 v71, v76 offset:236
	s_waitcnt lgkmcnt(10)
	v_add_f32_e32 v106, v106, v66
	v_add_f32_e32 v106, v106, v72
	s_waitcnt lgkmcnt(8)
	v_add_f32_e32 v107, v107, v67
	v_add_f32_e32 v107, v107, v73
	s_waitcnt lgkmcnt(6)
	v_add_f32_e32 v108, v108, v68
	v_add_f32_e32 v108, v108, v74
	s_waitcnt lgkmcnt(4)
	v_add_f32_e32 v109, v109, v69
	v_add_f32_e32 v109, v109, v75
	s_waitcnt lgkmcnt(2)
	v_add_f32_e32 v110, v110, v64
	v_add_f32_e32 v110, v110, v70
	s_waitcnt lgkmcnt(0)
	v_add_f32_e32 v111, v111, v65
	v_add_f32_e32 v111, v111, v71
	s_branch .LBB0_659

.LBB0_672:
	s_cmp_lt_u32 s50, 3
	s_cbranch_scc1 .LBB0_706
	s_add_i32 s6, s23, s90
	s_add_i32 s6, s6, -7
	s_cmp_gt_u32 s6, 7
	s_cselect_b64 vcc, -1, 0
	s_cbranch_scc1 .Lna_allmask_3
	s_add_i32 s6, s23, s27
	s_max_i32 s6, s6, -7
	s_add_i32 s6, s6, 7
	s_min_u32 s6, s6, 14
	s_mulk_i32 s6, 0x7c
	v_add_u32_e32 v124, s6, v228
	v_mov_b32_e32 v122, v223
	v_lshlrev_b32_e32 v108, 2, v223
	v_add_u32_e32 v108, 0x16100, v108
	ds_read_b32 v96, v124
	ds_read_b32 v102, v108
	ds_read_b32 v97, v124 offset:4
	ds_read_b32 v103, v108 offset:4
	ds_read_b32 v98, v124 offset:8
	ds_read_b32 v104, v108 offset:8
	ds_read_b32 v99, v124 offset:12
	ds_read_b32 v105, v108 offset:12
	ds_read_b32 v100, v124 offset:32
	ds_read_b32 v106, v108 offset:32
	ds_read_b32 v101, v124 offset:36
	ds_read_b32 v107, v108 offset:36
	s_waitcnt lgkmcnt(10)
	v_add_f32_e32 v80, v80, v96
	v_add_f32_e32 v80, v80, v102
	ds_read_b32 v96, v124 offset:40
	ds_read_b32 v102, v108 offset:40
	s_waitcnt lgkmcnt(10)
	v_add_f32_e32 v81, v81, v97
	v_add_f32_e32 v81, v81, v103
	ds_read_b32 v97, v124 offset:44
	ds_read_b32 v103, v108 offset:44
	s_waitcnt lgkmcnt(10)
	v_add_f32_e32 v82, v82, v98
	v_add_f32_e32 v82, v82, v104
	ds_read_b32 v98, v124 offset:64
	ds_read_b32 v104, v108 offset:64
	s_waitcnt lgkmcnt(10)
	v_add_f32_e32 v83, v83, v99
	v_add_f32_e32 v83, v83, v105
	ds_read_b32 v99, v124 offset:68
	ds_read_b32 v105, v108 offset:68
	s_waitcnt lgkmcnt(10)
	v_add_f32_e32 v84, v84, v100
	v_add_f32_e32 v84, v84, v106
	ds_read_b32 v100, v124 offset:72
	ds_read_b32 v106, v108 offset:72
	s_waitcnt lgkmcnt(10)
	v_add_f32_e32 v85, v85, v101
	v_add_f32_e32 v85, v85, v107
	ds_read_b32 v101, v124 offset:76
	ds_read_b32 v107, v108 offset:76
	s_waitcnt lgkmcnt(10)
	v_add_f32_e32 v86, v86, v96
	v_add_f32_e32 v86, v86, v102
	ds_read_b32 v96, v124 offset:96
	ds_read_b32 v102, v108 offset:96
	s_waitcnt lgkmcnt(10)
	v_add_f32_e32 v87, v87, v97
	v_add_f32_e32 v87, v87, v103
	ds_read_b32 v97, v124 offset:100
	ds_read_b32 v103, v108 offset:100
	s_waitcnt lgkmcnt(10)
	v_add_f32_e32 v88, v88, v98
	v_add_f32_e32 v88, v88, v104
	ds_read_b32 v98, v124 offset:104
	ds_read_b32 v104, v108 offset:104
	s_waitcnt lgkmcnt(10)
	v_add_f32_e32 v89, v89, v99
	v_add_f32_e32 v89, v89, v105
	ds_read_b32 v99, v124 offset:108
	ds_read_b32 v105, v108 offset:108
	s_waitcnt lgkmcnt(10)
	v_add_f32_e32 v90, v90, v100
	v_add_f32_e32 v90, v90, v106
	ds_read_b32 v100, v124 offset:128
	ds_read_b32 v106, v108 offset:128
	s_waitcnt lgkmcnt(10)
	v_add_f32_e32 v91, v91, v101
	v_add_f32_e32 v91, v91, v107
	ds_read_b32 v101, v124 offset:132
	ds_read_b32 v107, v108 offset:132
	s_waitcnt lgkmcnt(10)
	v_add_f32_e32 v92, v92, v96
	v_add_f32_e32 v92, v92, v102
	ds_read_b32 v96, v124 offset:136
	ds_read_b32 v102, v108 offset:136
	s_waitcnt lgkmcnt(10)
	v_add_f32_e32 v93, v93, v97
	v_add_f32_e32 v93, v93, v103
	ds_read_b32 v97, v124 offset:140
	ds_read_b32 v103, v108 offset:140
	s_waitcnt lgkmcnt(10)
	v_add_f32_e32 v94, v94, v98
	v_add_f32_e32 v94, v94, v104
	ds_read_b32 v98, v124 offset:160
	ds_read_b32 v104, v108 offset:160
	s_waitcnt lgkmcnt(10)
	v_add_f32_e32 v95, v95, v99
	v_add_f32_e32 v95, v95, v105
	ds_read_b32 v99, v124 offset:164
	ds_read_b32 v105, v108 offset:164
	s_waitcnt lgkmcnt(10)
	v_add_f32_e32 v64, v64, v100
	v_add_f32_e32 v64, v64, v106
	ds_read_b32 v100, v124 offset:168
	ds_read_b32 v106, v108 offset:168
	s_waitcnt lgkmcnt(10)
	v_add_f32_e32 v65, v65, v101
	v_add_f32_e32 v65, v65, v107
	ds_read_b32 v101, v124 offset:172
	ds_read_b32 v107, v108 offset:172
	s_waitcnt lgkmcnt(10)
	v_add_f32_e32 v66, v66, v96
	v_add_f32_e32 v66, v66, v102
	ds_read_b32 v96, v124 offset:192
	ds_read_b32 v102, v108 offset:192
	s_waitcnt lgkmcnt(10)
	v_add_f32_e32 v67, v67, v97
	v_add_f32_e32 v67, v67, v103
	ds_read_b32 v97, v124 offset:196
	ds_read_b32 v103, v108 offset:196
	s_waitcnt lgkmcnt(10)
	v_add_f32_e32 v68, v68, v98
	v_add_f32_e32 v68, v68, v104
	ds_read_b32 v98, v124 offset:200
	ds_read_b32 v104, v108 offset:200
	s_waitcnt lgkmcnt(10)
	v_add_f32_e32 v69, v69, v99
	v_add_f32_e32 v69, v69, v105
	ds_read_b32 v99, v124 offset:204
	ds_read_b32 v105, v108 offset:204
	s_waitcnt lgkmcnt(10)
	v_add_f32_e32 v70, v70, v100
	v_add_f32_e32 v70, v70, v106
	ds_read_b32 v100, v124 offset:224
	ds_read_b32 v106, v108 offset:224
	s_waitcnt lgkmcnt(10)
	v_add_f32_e32 v71, v71, v101
	v_add_f32_e32 v71, v71, v107
	ds_read_b32 v101, v124 offset:228
	ds_read_b32 v107, v108 offset:228
	s_waitcnt lgkmcnt(10)
	v_add_f32_e32 v72, v72, v96
	v_add_f32_e32 v72, v72, v102
	ds_read_b32 v96, v124 offset:232
	ds_read_b32 v102, v108 offset:232
	s_waitcnt lgkmcnt(10)
	v_add_f32_e32 v73, v73, v97
	v_add_f32_e32 v73, v73, v103
	ds_read_b32 v97, v124 offset:236
	ds_read_b32 v103, v108 offset:236
	s_waitcnt lgkmcnt(10)
	v_add_f32_e32 v74, v74, v98
	v_add_f32_e32 v74, v74, v104
	s_waitcnt lgkmcnt(8)
	v_add_f32_e32 v75, v75, v99
	v_add_f32_e32 v75, v75, v105
	s_waitcnt lgkmcnt(6)
	v_add_f32_e32 v76, v76, v100
	v_add_f32_e32 v76, v76, v106
	s_waitcnt lgkmcnt(4)
	v_add_f32_e32 v77, v77, v101
	v_add_f32_e32 v77, v77, v107
	s_waitcnt lgkmcnt(2)
	v_add_f32_e32 v78, v78, v96
	v_add_f32_e32 v78, v78, v102
	s_waitcnt lgkmcnt(0)
	v_add_f32_e32 v79, v79, v97
	v_add_f32_e32 v79, v79, v103
	s_branch .LBB0_706

.LBB0_737:
	v_add_u32_e32 v0, s81, v226
	ds_read_b64_tr_b16 v[6:7], v0 offset:24576
	ds_read_b64_tr_b16 v[8:9], v0 offset:25088
	s_waitcnt lgkmcnt(9)
	v_mfma_f32_32x32x16_bf16 v[96:111], v[188:191], v[156:159], v[48:63]
	v_add_f32_e32 v2, v80, v81
	v_add_f32_e32 v2, v82, v2
	v_add_f32_e32 v2, v83, v2
	v_add_f32_e32 v2, v84, v2
	v_add_f32_e32 v10, v85, v2
	v_cvt_pk_bf16_f32 v140, v80, v81
	v_cvt_pk_bf16_f32 v141, v82, v83
	ds_read_b64_tr_b16 v[2:3], v0 offset:28672
	ds_read_b64_tr_b16 v[4:5], v0 offset:29184
	s_waitcnt lgkmcnt(10)
	v_mfma_f32_32x32x16_bf16 v[48:63], v[184:187], v[156:159], v[48:63]
	v_add_f32_e32 v10, v86, v10
	v_add_f32_e32 v10, v87, v10
	v_add_f32_e32 v10, v88, v10
	v_add_f32_e32 v14, v89, v10
	v_cvt_pk_bf16_f32 v142, v84, v85
	v_cvt_pk_bf16_f32 v143, v86, v87
	ds_read_b64_tr_b16 v[10:11], v0 offset:25600
	ds_read_b64_tr_b16 v[12:13], v0 offset:26112
	s_waitcnt lgkmcnt(11)
	v_mfma_f32_32x32x16_bf16 v[96:111], v[180:183], v[152:155], v[96:111]
	v_add_f32_e32 v14, v90, v14
	v_add_f32_e32 v14, v91, v14
	v_add_f32_e32 v14, v92, v14
	v_add_f32_e32 v14, v93, v14
	v_cvt_pk_bf16_f32 v136, v88, v89
	v_cvt_pk_bf16_f32 v137, v90, v91
	ds_read_b64_tr_b16 v[80:81], v0 offset:29696
	ds_read_b64_tr_b16 v[82:83], v0 offset:30208
	s_waitcnt lgkmcnt(12)
	v_mfma_f32_32x32x16_bf16 v[48:63], v[176:179], v[152:155], v[48:63]
	v_add_f32_e32 v14, v94, v14
	v_add_f32_e32 v14, v95, v14
	v_add_f32_e32 v14, v64, v14
	v_add_f32_e32 v14, v65, v14
	v_cvt_pk_bf16_f32 v138, v92, v93
	v_cvt_pk_bf16_f32 v139, v94, v95
	ds_read_b64_tr_b16 v[84:85], v0 offset:26624
	ds_read_b64_tr_b16 v[86:87], v0 offset:27136
	s_waitcnt lgkmcnt(13)
	v_mfma_f32_32x32x16_bf16 v[96:111], v[172:175], v[148:151], v[96:111]
	v_add_f32_e32 v14, v66, v14
	v_add_f32_e32 v14, v67, v14
	v_add_f32_e32 v14, v68, v14
	v_add_f32_e32 v14, v69, v14
	v_cvt_pk_bf16_f32 v132, v64, v65
	v_cvt_pk_bf16_f32 v133, v66, v67
	ds_read_b64_tr_b16 v[88:89], v0 offset:30720
	ds_read_b64_tr_b16 v[90:91], v0 offset:31232
	s_waitcnt lgkmcnt(14)
	v_mfma_f32_32x32x16_bf16 v[48:63], v[168:171], v[148:151], v[48:63]
	v_add_f32_e32 v14, v70, v14
	v_add_f32_e32 v14, v71, v14
	v_add_f32_e32 v14, v72, v14
	v_add_f32_e32 v14, v73, v14
	v_cvt_pk_bf16_f32 v134, v68, v69
	v_cvt_pk_bf16_f32 v135, v70, v71
	ds_read_b64_tr_b16 v[92:93], v0 offset:27648
	ds_read_b64_tr_b16 v[94:95], v0 offset:28160
	s_waitcnt lgkmcnt(14)
	v_mfma_f32_32x32x16_bf16 v[96:111], v[164:167], v[144:147], v[96:111]
	v_add_f32_e32 v14, v74, v14
	v_add_f32_e32 v14, v75, v14
	v_add_f32_e32 v14, v76, v14
	v_add_f32_e32 v14, v77, v14
	v_cvt_pk_bf16_f32 v128, v72, v73
	v_cvt_pk_bf16_f32 v129, v74, v75
	ds_read_b64_tr_b16 v[112:113], v0 offset:31744
	ds_read_b64_tr_b16 v[114:115], v0 offset:32256
	v_mfma_f32_32x32x16_bf16 v[48:63], v[160:163], v[144:147], v[48:63]
	v_add_f32_e32 v0, v78, v14
	v_add_f32_e32 v0, v79, v0
	v_add_f32_e32 v0, 0, v0
	v_cvt_pk_bf16_f32 v130, v76, v77
	v_cvt_pk_bf16_f32 v131, v78, v79
	s_cmp_lt_i32 s0, 5
	s_cbranch_scc1 .LBB0_771
	s_add_i32 s65, s65, s63
	s_max_i32 s0, s65, 4
	s_add_i32 s0, s0, -4
	s_min_u32 s0, s0, 56
	s_add_i32 s13, s13, s12
	s_sub_i32 s0, s13, s0
	s_cmp_gt_u32 s0, 7
	s_cselect_b64 vcc, -1, 0
	s_cbranch_scc1 .Lna_allmask_4
	s_sub_i32 s0, s13, s65
	s_max_i32 s0, s0, -7
	s_add_i32 s0, s0, 7
	s_min_u32 s0, s0, 14
	s_mulk_i32 s0, 0x7c
	v_lshlrev_b32_e32 v14, 2, v224
	v_add3_u32 v116, v225, s0, v14
	v_lshlrev_b32_e32 v76, 2, v223
	v_add_u32_e32 v76, 0x16100, v76
	ds_read_b32 v64, v116
	ds_read_b32 v70, v76
	ds_read_b32 v65, v116 offset:4
	ds_read_b32 v71, v76 offset:4
	ds_read_b32 v66, v116 offset:8
	ds_read_b32 v72, v76 offset:8
	ds_read_b32 v67, v116 offset:12
	ds_read_b32 v73, v76 offset:12
	ds_read_b32 v68, v116 offset:32
	ds_read_b32 v74, v76 offset:32
	ds_read_b32 v69, v116 offset:36
	ds_read_b32 v75, v76 offset:36
	s_waitcnt lgkmcnt(10)
	v_add_f32_e32 v96, v96, v64
	v_add_f32_e32 v96, v96, v70
	ds_read_b32 v64, v116 offset:40
	ds_read_b32 v70, v76 offset:40
	s_waitcnt lgkmcnt(10)
	v_add_f32_e32 v97, v97, v65
	v_add_f32_e32 v97, v97, v71
	ds_read_b32 v65, v116 offset:44
	ds_read_b32 v71, v76 offset:44
	s_waitcnt lgkmcnt(10)
	v_add_f32_e32 v98, v98, v66
	v_add_f32_e32 v98, v98, v72
	ds_read_b32 v66, v116 offset:64
	ds_read_b32 v72, v76 offset:64
	s_waitcnt lgkmcnt(10)
	v_add_f32_e32 v99, v99, v67
	v_add_f32_e32 v99, v99, v73
	ds_read_b32 v67, v116 offset:68
	ds_read_b32 v73, v76 offset:68
	s_waitcnt lgkmcnt(10)
	v_add_f32_e32 v100, v100, v68
	v_add_f32_e32 v100, v100, v74
	ds_read_b32 v68, v116 offset:72
	ds_read_b32 v74, v76 offset:72
	s_waitcnt lgkmcnt(10)
	v_add_f32_e32 v101, v101, v69
	v_add_f32_e32 v101, v101, v75
	ds_read_b32 v69, v116 offset:76
	ds_read_b32 v75, v76 offset:76
	s_waitcnt lgkmcnt(10)
	v_add_f32_e32 v102, v102, v64
	v_add_f32_e32 v102, v102, v70
	ds_read_b32 v64, v116 offset:96
	ds_read_b32 v70, v76 offset:96
	s_waitcnt lgkmcnt(10)
	v_add_f32_e32 v103, v103, v65
	v_add_f32_e32 v103, v103, v71
	ds_read_b32 v65, v116 offset:100
	ds_read_b32 v71, v76 offset:100
	s_waitcnt lgkmcnt(10)
	v_add_f32_e32 v104, v104, v66
	v_add_f32_e32 v104, v104, v72
	ds_read_b32 v66, v116 offset:104
	ds_read_b32 v72, v76 offset:104
	s_waitcnt lgkmcnt(10)
	v_add_f32_e32 v105, v105, v67
	v_add_f32_e32 v105, v105, v73
	ds_read_b32 v67, v116 offset:108
	ds_read_b32 v73, v76 offset:108
	s_waitcnt lgkmcnt(10)
	v_add_f32_e32 v106, v106, v68
	v_add_f32_e32 v106, v106, v74
	ds_read_b32 v68, v116 offset:128
	ds_read_b32 v74, v76 offset:128
	s_waitcnt lgkmcnt(10)
	v_add_f32_e32 v107, v107, v69
	v_add_f32_e32 v107, v107, v75
	ds_read_b32 v69, v116 offset:132
	ds_read_b32 v75, v76 offset:132
	s_waitcnt lgkmcnt(10)
	v_add_f32_e32 v108, v108, v64
	v_add_f32_e32 v108, v108, v70
	ds_read_b32 v64, v116 offset:136
	ds_read_b32 v70, v76 offset:136
	s_waitcnt lgkmcnt(10)
	v_add_f32_e32 v109, v109, v65
	v_add_f32_e32 v109, v109, v71
	ds_read_b32 v65, v116 offset:140
	ds_read_b32 v71, v76 offset:140
	s_waitcnt lgkmcnt(10)
	v_add_f32_e32 v110, v110, v66
	v_add_f32_e32 v110, v110, v72
	ds_read_b32 v66, v116 offset:160
	ds_read_b32 v72, v76 offset:160
	s_waitcnt lgkmcnt(10)
	v_add_f32_e32 v111, v111, v67
	v_add_f32_e32 v111, v111, v73
	ds_read_b32 v67, v116 offset:164
	ds_read_b32 v73, v76 offset:164
	s_waitcnt lgkmcnt(10)
	v_add_f32_e32 v48, v48, v68
	v_add_f32_e32 v48, v48, v74
	ds_read_b32 v68, v116 offset:168
	ds_read_b32 v74, v76 offset:168
	s_waitcnt lgkmcnt(10)
	v_add_f32_e32 v49, v49, v69
	v_add_f32_e32 v49, v49, v75
	ds_read_b32 v69, v116 offset:172
	ds_read_b32 v75, v76 offset:172
	s_waitcnt lgkmcnt(10)
	v_add_f32_e32 v50, v50, v64
	v_add_f32_e32 v50, v50, v70
	ds_read_b32 v64, v116 offset:192
	ds_read_b32 v70, v76 offset:192
	s_waitcnt lgkmcnt(10)
	v_add_f32_e32 v51, v51, v65
	v_add_f32_e32 v51, v51, v71
	ds_read_b32 v65, v116 offset:196
	ds_read_b32 v71, v76 offset:196
	s_waitcnt lgkmcnt(10)
	v_add_f32_e32 v52, v52, v66
	v_add_f32_e32 v52, v52, v72
	ds_read_b32 v66, v116 offset:200
	ds_read_b32 v72, v76 offset:200
	s_waitcnt lgkmcnt(10)
	v_add_f32_e32 v53, v53, v67
	v_add_f32_e32 v53, v53, v73
	ds_read_b32 v67, v116 offset:204
	ds_read_b32 v73, v76 offset:204
	s_waitcnt lgkmcnt(10)
	v_add_f32_e32 v54, v54, v68
	v_add_f32_e32 v54, v54, v74
	ds_read_b32 v68, v116 offset:224
	ds_read_b32 v74, v76 offset:224
	s_waitcnt lgkmcnt(10)
	v_add_f32_e32 v55, v55, v69
	v_add_f32_e32 v55, v55, v75
	ds_read_b32 v69, v116 offset:228
	ds_read_b32 v75, v76 offset:228
	s_waitcnt lgkmcnt(10)
	v_add_f32_e32 v56, v56, v64
	v_add_f32_e32 v56, v56, v70
	ds_read_b32 v64, v116 offset:232
	ds_read_b32 v70, v76 offset:232
	s_waitcnt lgkmcnt(10)
	v_add_f32_e32 v57, v57, v65
	v_add_f32_e32 v57, v57, v71
	ds_read_b32 v65, v116 offset:236
	ds_read_b32 v71, v76 offset:236
	s_waitcnt lgkmcnt(10)
	v_add_f32_e32 v58, v58, v66
	v_add_f32_e32 v58, v58, v72
	s_waitcnt lgkmcnt(8)
	v_add_f32_e32 v59, v59, v67
	v_add_f32_e32 v59, v59, v73
	s_waitcnt lgkmcnt(6)
	v_add_f32_e32 v60, v60, v68
	v_add_f32_e32 v60, v60, v74
	s_waitcnt lgkmcnt(4)
	v_add_f32_e32 v61, v61, v69
	v_add_f32_e32 v61, v61, v75
	s_waitcnt lgkmcnt(2)
	v_add_f32_e32 v62, v62, v64
	v_add_f32_e32 v62, v62, v70
	s_waitcnt lgkmcnt(0)
	v_add_f32_e32 v63, v63, v65
	v_add_f32_e32 v63, v63, v71
	s_branch .LBB0_771
